# GQA unit prologue: tile 1-2 loads issued without draining tile 0 first (counted waits only)
# baseline (speedup 1.0000x reference)
; #define SLOAD(i, j) do { const int _row = KROW(j); skn[i] = *(const bf16x8*)(Knp + (size_t)(_row + sr) * ldk + c8 * 8); sv[i] = *(const bf16x8*)(Vp + (size_t)(_row + sr) * ldv + c8 * 8); \
;         if (krw) skr[i] = *(const bf16x8*)(Krp + (size_t)(_row + sr2) * 32 + c4 * 8); } while (0)
; #define SWRITE(b, i) do { *(LAS bf16x8*)(lds + (b) * BUF + kn_st) = skn[i]; *(LAS bf16x8*)(lds + (b) * BUF + v_stw) = sv[i]; if (krw) *(LAS bf16x8*)(lds + (b) * BUF + kr_st) = skr[i]; } while (0)
; #define SWRITEO(boff, i) do { *(LAS bf16x8*)(lds + (boff) + kn_st) = skn[i]; *(LAS bf16x8*)(lds + (boff) + v_stw) = sv[i]; if (krw) *(LAS bf16x8*)(lds + (boff) + kr_st) = skr[i]; } while (0)
; #define SWAIT() asm volatile("s_waitcnt vmcnt(2)" ::: "memory")
; template <int DQK, bool FIXM> ...
;     ...
;     const int wid = tid >> 6, lane = tid & 63, r32 = lane & 31, hi = lane >> 5;
;     float m_reg = 0.f, l_reg = 0.f; f32x16 o0 = {}, o1 = {}, negm = {}; bf16x8 qr[NQ];
;     if (FIXM) { _Pragma("unroll") for (int r = 0; r < 16; ++r) negm[r] = -mfix; }
;     const bf16_t* Qw = Qp + (size_t)(wid * 32 + r32) * ldq + hi * 8;
; #pragma unroll
;     for (int d0 = 0; d0 < NQ; ++d0) qr[d0] = *(const bf16x8*)(Qw + d0 * 16);
;     ...
;     __syncthreads();
;     SLOAD(0, 0); asm volatile("s_waitcnt vmcnt(0)" ::: "memory"); SWRITE(0, 0);
;     SLOAD(1, 1); if (2 < NT) SLOAD(0, 2);
;     __syncthreads();
;     qkt<DQK>(pA0, pA1, lds, qr, r32, hi, negm);
;     if (FIXM) { alA = 1.f; _Pragma("unroll") for (int r = 0; r < 16; ++r) pA0[r] = __builtin_amdgcn_exp2f(pA0[r]); } else partialSM<true>(pA0, pA1, m_reg, negm, alA);
;     SWAIT(); SWRITEO(BUF, 1);
.LBB0_496:
	s_lshr_b32 s8, s8, 6
	s_and_b64 s[0:1], s[10:11], exec
	s_cselect_b32 s8, s8, s14
	s_and_b32 s9, s8, 7
	s_lshl_b64 s[0:1], s[4:5], 10
	s_add_u32 s0, s15, s0
	s_addc_u32 s1, s16, s1
	s_lshl_b32 s34, s9, 6
	s_lshl_b32 s9, s9, 7
	s_add_u32 s38, s0, s9
	s_addc_u32 s39, s1, 0
	s_lshl_b32 s0, s8, 5
	s_and_b32 s8, s0, 0x80
	s_add_u32 s0, s19, s8
	v_add_u32_e32 v16, s36, v1
	s_addc_u32 s1, s20, 0
	v_ashrrev_i32_e32 v17, 31, v16
	s_add_u32 s8, s23, s8
	v_lshl_add_u64 v[4:5], s[38:39], 0, v[192:193]
	v_lshlrev_b32_e32 v2, 1, v200
	v_lshlrev_b64 v[16:17], 8, v[16:17]
	s_addc_u32 s9, s24, 0
	v_lshl_add_u64 v[4:5], v[4:5], 0, v[2:3]
	v_lshl_add_u64 v[34:35], s[0:1], 0, v[16:17]
	v_lshlrev_b32_e32 v2, 1, v188
	v_lshl_add_u64 v[34:35], v[34:35], 0, v[2:3]
	v_lshl_add_u64 v[16:17], s[8:9], 0, v[16:17]
	global_load_dwordx4 v[114:117], v[4:5], off
	global_load_dwordx4 v[12:15], v[4:5], off offset:32
	global_load_dwordx4 v[8:11], v[4:5], off offset:64
	s_nop 0
	global_load_dwordx4 v[4:7], v[4:5], off offset:96
	s_barrier
	v_lshl_add_u64 v[16:17], v[16:17], 0, v[2:3]
	global_load_dwordx4 v[34:37], v[34:35], off
	s_nop 0
	global_load_dwordx4 v[38:41], v[16:17], off
	s_lshl_b32 s36, s31, 6
	s_sub_i32 s36, s29, s36
	s_and_b64 s[10:11], s[10:11], exec
	s_cselect_b32 s10, s12, s36
	v_add_u32_e32 v16, s10, v191
	v_ashrrev_i32_e32 v17, 31, v16
	v_lshlrev_b64 v[16:17], 8, v[16:17]
	v_add_u32_e32 v42, s10, v189
	v_lshl_add_u64 v[44:45], s[0:1], 0, v[16:17]
	v_lshl_add_u64 v[16:17], s[8:9], 0, v[16:17]
	v_lshl_add_u64 v[44:45], v[44:45], 0, v[2:3]
	v_lshl_add_u64 v[16:17], v[16:17], 0, v[2:3]
	v_ashrrev_i32_e32 v43, 31, v42
	global_load_dwordx4 v[58:61], v[44:45], off
	global_load_dwordx4 v[62:65], v[16:17], off
	v_lshlrev_b64 v[16:17], 8, v[42:43]
	v_lshl_add_u64 v[42:43], s[0:1], 0, v[16:17]
	v_lshl_add_u64 v[16:17], s[8:9], 0, v[16:17]
	v_lshl_add_u64 v[42:43], v[42:43], 0, v[2:3]
	v_lshl_add_u64 v[16:17], v[16:17], 0, v[2:3]
	global_load_dwordx4 v[118:121], v[42:43], off
	global_load_dwordx4 v[122:125], v[16:17], off
	v_add_u32_e32 v106, 0, v187
	v_add_u32_e32 v46, v208, v209
	v_add_u32_e32 v107, 0, v214
	v_add_u32_e32 v16, v208, v210
	v_add_u32_e32 v17, v208, v211
	v_add_u32_e32 v57, v208, v212
	v_mov_b32_e32 v136, 0
	s_mov_b32 s10, 0xa000
	s_movk_i32 s11, 0x5000
	v_mov_b32_e32 v137, v221
	v_mov_b32_e32 v50, 0
	v_mov_b32_e32 v42, v136
	v_mov_b32_e32 v43, v136
	v_mov_b32_e32 v48, v136
	v_mov_b32_e32 v49, v136
	v_mov_b32_e32 v51, v136
	v_mov_b32_e32 v56, v136
	v_lshl_add_u64 v[134:135], s[8:9], 0, v[2:3]
	s_mov_b64 s[44:45], s[8:9]
	s_waitcnt vmcnt(5)
	ds_write_b128 v106, v[34:37]
	s_waitcnt vmcnt(4)
	ds_write_b128 v107, v[38:41] offset:12288
	s_waitcnt lgkmcnt(0)
	s_barrier
	ds_read_b128 v[34:37], v46
	ds_read_b128 v[38:41], v46 offset:4096
	s_waitcnt lgkmcnt(1)
	v_mfma_f32_32x32x16_bf16 v[82:97], v[34:37], v[114:117], v[18:33]
	ds_read_b128 v[34:37], v16
	ds_read_b128 v[44:47], v17
	ds_read_b128 v[52:55], v17 offset:4096
	ds_read_b128 v[98:101], v57
	ds_read_b128 v[102:105], v57 offset:4096
	v_mov_b32_e32 v57, v136
	s_waitcnt lgkmcnt(5)
	v_mfma_f32_32x32x16_bf16 v[66:81], v[38:41], v[114:117], v[18:33]
	ds_read_b128 v[38:41], v16 offset:4096
	s_waitcnt vmcnt(2)
	v_lshl_add_u64 v[16:17], s[0:1], 0, v[2:3]
	s_mov_b64 s[42:43], s[0:1]
	s_add_i32 s0, s30, -1
	s_waitcnt vmcnt(3)
	ds_write_b128 v106, v[58:61] offset:20480
	s_waitcnt vmcnt(2)
	ds_write_b128 v107, v[62:65] offset:32768
	v_mov_b32_e32 v58, v136
	v_mov_b32_e32 v59, v136
	s_waitcnt lgkmcnt(7)
	v_mfma_f32_32x32x16_bf16 v[82:97], v[34:37], v[12:15], v[82:97]
	v_mov_b32_e32 v34, 0
	v_mov_b32_e32 v35, v136
	v_mov_b32_e32 v36, v136
	v_mov_b32_e32 v37, v136
	v_mov_b32_e32 v60, v136
	v_mov_b32_e32 v61, v136
	v_mov_b32_e32 v62, v136
	s_waitcnt lgkmcnt(2)
	v_mfma_f32_32x32x16_bf16 v[66:81], v[38:41], v[12:15], v[66:81]
	v_mov_b32_e32 v38, v136
	v_mov_b32_e32 v39, v136
	v_mov_b32_e32 v40, v136
	v_mov_b32_e32 v41, v136
	v_mov_b32_e32 v63, v136
	v_mov_b32_e32 v64, v136
	v_mov_b32_e32 v65, v136
	v_mfma_f32_32x32x16_bf16 v[82:97], v[44:47], v[8:11], v[82:97]
	v_mov_b32_e32 v44, v136
	v_mov_b32_e32 v45, v136
	v_mov_b32_e32 v46, v136
	v_mov_b32_e32 v47, v136
	v_mfma_f32_32x32x16_bf16 v[66:81], v[52:55], v[8:11], v[66:81]
	v_mov_b32_e32 v52, v136
	v_mov_b32_e32 v53, v136
	v_mov_b32_e32 v54, v136
	v_mov_b32_e32 v55, v136
	v_mfma_f32_32x32x16_bf16 v[82:97], v[98:101], v[4:7], v[82:97]
	v_mfma_f32_32x32x16_bf16 v[66:81], v[102:105], v[4:7], v[66:81]
	s_nop 10
	v_exp_f32_e32 v143, v82
	v_exp_f32_e32 v145, v83
	v_exp_f32_e32 v141, v84
	v_exp_f32_e32 v144, v85
	v_exp_f32_e32 v139, v86
	v_exp_f32_e32 v142, v87
	v_exp_f32_e32 v138, v88
	v_exp_f32_e32 v140, v89
	v_exp_f32_e32 v151, v90
	v_exp_f32_e32 v153, v91
	v_exp_f32_e32 v149, v92
	v_exp_f32_e32 v152, v93
	v_exp_f32_e32 v147, v94
	v_exp_f32_e32 v150, v95
	v_exp_f32_e32 v146, v96
	v_exp_f32_e32 v148, v97
	v_add_u32_e32 v223, v208, v209
	v_add_u32_e32 v252, v208, v210
	v_add_u32_e32 v253, v208, v211
	v_lshlrev_b32_e32 v137, 8, v221
	v_add_u32_e32 v137, v137, v2
	v_add_u32_e32 v2, v208, v212
